# speedup vs baseline: 1.0266x; 1.0235x over previous
.LBB0_3:
	s_sub_u32 s3, s2, 0x5200
	s_cbranch_scc1 .Lcvt_not_wo
	s_cmpk_lt_u32 s3, 0x100
	s_cbranch_scc0 .LBB0_2
	s_load_dwordx2 s[4:5], s[0:1], 0x20
	s_load_dwordx2 s[6:7], s[0:1], 0x38
	s_lshl_b32 s8, s3, 17
	v_cmp_eq_u32_e32 vcc, 0, v0
	v_mov_b32_e32 v1, 0
	s_waitcnt lgkmcnt(0)
	s_add_u32 s6, s6, s8
	s_addc_u32 s7, s7, 0
	v_mov_b32_e32 v2, s4
	v_mov_b32_e32 v3, s5
	s_and_saveexec_b64 s[8:9], vcc
	s_cbranch_execz .LBB0_2
	global_store_dwordx2 v1, v[2:3], s[6:7]
	s_endpgm

_Z11attn_kernelPKDF16_PDF16_:
	s_cmpk_gt_i32 s2, 0xff
	s_movk_i32 s4, 0xff
	s_cbranch_scc1 .Lattn_early_exit
	s_load_dwordx4 s[8:11], s[0:1], 0x0
	v_lshlrev_b32_e32 v254, 5, v0
	v_lshlrev_b32_e32 v255, 4, v0
	s_mov_b32 s58, 0
	s_mov_b32 s59, 0
	s_load_dword s3, s[0:1], 0x10
	v_cmp_lt_u32_e32 vcc, s4, v0
	s_and_saveexec_b64 s[0:1], vcc
	s_setprio 1
	s_or_b64 exec, exec, s[0:1]
	s_ashr_i32 s1, s2, 3
	s_lshr_b32 s4, s1, 28
	s_add_i32 s4, s1, s4
	s_ashr_i32 s5, s4, 4
	s_and_b32 s6, s4, -16
	s_and_b32 s0, s2, 7
	s_sub_i32 s12, s1, s6
	s_lshl_b32 s1, s5, 3
	s_or_b32 s6, s1, s0
	s_lshr_b32 s0, s4, 29
	s_add_i32 s1, s6, s0
	s_lshl_b32 s4, s6, 2
	s_ashr_i32 s0, s1, 3
	s_and_b32 s1, s1, 0x7ffff8
	s_ashr_i32 s5, s4, 31
	s_sub_i32 s19, 31, s12
	s_sub_i32 s7, s6, s1
	s_ashr_i32 s13, s12, 31
	s_lshl_b64 s[4:5], s[4:5], 19
	s_waitcnt lgkmcnt(0)
	s_sub_u32 s56, s8, 0x2000000
	s_subb_u32 s57, s9, 0
	s_lshl_b32 s60, s2, 17
	s_add_u32 s56, s56, s60
	s_addc_u32 s57, s57, 0
	s_load_dwordx2 s[54:55], s[56:57], 0x0
	s_lshl_b32 s60, s2, 18
	s_add_u32 s1, s8, s4
	s_addc_u32 s14, s9, s5
	s_lshl_b64 s[4:5], s[12:13], 14
	s_add_u32 s33, s1, s4
	s_addc_u32 s36, s14, s5
	s_ashr_i32 s1, s0, 31
	s_lshl_b64 s[0:1], s[0:1], 24
	s_add_u32 s4, s10, s0
	s_addc_u32 s5, s11, s1
	s_lshl_b64 s[0:1], s[12:13], 19
	s_add_u32 s4, s4, s0
	s_addc_u32 s5, s5, s1
	s_lshl_b32 s0, s7, 9
	s_ashr_i32 s1, s0, 31
	s_lshl_b64 s[0:1], s[0:1], 1
	s_add_u32 s16, s4, s0
	s_addc_u32 s17, s5, s1
	s_add_u32 s13, s8, 0x2000000
	s_addc_u32 s37, s9, 0
	s_ashr_i32 s7, s6, 31
	s_lshl_b64 s[0:1], s[6:7], 19
	s_add_u32 s28, s13, s0
	s_addc_u32 s29, s37, s1
	v_lshlrev_b32_e32 v2, 4, v0
	v_mov_b32_e32 v3, 0
	s_add_u32 s38, s8, 0x2800000
	s_movk_i32 s4, 0x2000
	v_lshl_add_u64 v[4:5], s[28:29], 0, v[2:3]
	s_addc_u32 s39, s9, 0
	v_add_co_u32_e32 v4, vcc, s4, v4
	s_add_u32 s30, s38, s0
	s_nop 0
	v_addc_co_u32_e32 v5, vcc, 0, v5, vcc
	s_addc_u32 s31, s39, s1
	global_load_dwordx4 v[186:189], v2, s[28:29]
	global_load_dwordx4 v[190:193], v[4:5], off
	v_lshl_add_u64 v[4:5], s[30:31], 0, v[2:3]
	v_add_co_u32_e32 v4, vcc, s4, v4
	v_readfirstlane_b32 s4, v0
	s_nop 0
	v_addc_co_u32_e32 v5, vcc, 0, v5, vcc
	global_load_dwordx4 v[178:181], v[4:5], off
	v_lshlrev_b32_e32 v1, 7, v0
	v_lshrrev_b32_e32 v4, 2, v0
	s_movk_i32 s0, 0xf88
	s_lshr_b32 s14, s4, 7
	s_mov_b32 s15, 0
	s_lshl_b32 s51, s12, 6
	v_bitop3_b32 v1, v1, s0, v4 bitop3:0xc8
	s_lshl_b64 s[0:1], s[14:15], 19
	s_add_u32 s0, s33, s0
	s_addc_u32 s1, s36, s1
	s_lshl_b32 s4, s4, 7
	s_and_b32 s4, s4, 0x2000
	s_add_u32 s0, s0, s4
	v_lshlrev_b32_e32 v1, 1, v1
	s_addc_u32 s1, s1, 0
	global_load_dwordx4 v[146:149], v1, s[0:1]
	global_load_dwordx4 v[150:153], v1, s[0:1] offset:32
	global_load_dwordx4 v[154:157], v1, s[0:1] offset:64
	global_load_dwordx4 v[158:161], v1, s[0:1] offset:96
	global_load_dwordx4 v[162:165], v1, s[0:1] offset:128
	global_load_dwordx4 v[166:169], v1, s[0:1] offset:160
	global_load_dwordx4 v[170:173], v1, s[0:1] offset:192
	global_load_dwordx4 v[174:177], v1, s[0:1] offset:224
	global_load_dwordx4 v[182:185], v2, s[30:31]
	v_and_b32_e32 v5, 0x70, v0
	s_movk_i32 s0, 0xf0
	v_and_b32_e32 v4, 0x1f00, v2
	v_bitop3_b32 v1, v2, v5, s0 bitop3:0x6c
	v_add3_u32 v1, 0, v4, v1
	v_lshrrev_b32_e32 v4, 5, v0
	v_lshrrev_b32_e32 v6, 4, v0
	v_lshrrev_b32_e32 v9, 3, v0
	v_bfe_u32 v12, v0, 4, 2
	v_and_b32_e32 v9, 8, v9
	v_and_or_b32 v4, v4, 4, v12
	v_or_b32_e32 v12, 32, v6
	v_lshlrev_b32_e32 v7, 3, v0
	v_and_or_b32 v10, v6, 16, v9
	v_and_or_b32 v9, v12, 48, v9
	v_and_b32_e32 v8, 0x78, v7
	v_lshrrev_b32_e32 v10, 1, v10
	v_bfe_u32 v11, v7, 5, 2
	v_lshrrev_b32_e32 v9, 1, v9
	v_or_b32_e32 v10, v10, v11
	v_lshlrev_b32_e32 v8, 1, v8
	v_or_b32_e32 v9, v9, v11
	v_lshlrev_b32_e32 v10, 9, v10
	v_lshlrev_b32_e32 v4, 6, v4
	v_and_b32_e32 v12, 48, v8
	v_lshlrev_b32_e32 v9, 9, v9
	v_lshlrev_b32_e32 v11, 1, v0
	v_or3_b32 v10, v10, v4, v12
	v_or3_b32 v4, v9, v4, v12
	v_and_b32_e32 v9, 0xc0, v2
	v_and_b32_e32 v11, 32, v11
	v_and_b32_e32 v7, 0x118, v7
	v_or3_b32 v7, v11, v9, v7
	v_bfe_u32 v9, v0, 5, 1
	s_cmp_lg_u32 0, -1
	v_lshlrev_b32_e32 v6, 8, v6
	s_cselect_b32 s0, 0, 0
	v_lshlrev_b32_e32 v200, 4, v9
	s_waitcnt vmcnt(0)
	s_waitcnt vmcnt(11)
	ds_write_b128 v1, v[186:189] offset:32768
	s_waitcnt vmcnt(10)
	ds_write_b128 v1, v[190:193] offset:40960
	v_and_b32_e32 v1, 31, v0
	v_lshlrev_b32_e32 v11, 2, v9
	v_bitop3_b32 v5, v8, v6, v5 bitop3:0xde
	v_add_u32_e32 v207, s0, v7
	v_or_b32_e32 v198, v8, v6
	v_and_b32_e32 v2, 0x70, v2
	v_or_b32_e32 v6, 32, v200
	v_or_b32_e32 v7, 64, v200
	v_or_b32_e32 v8, 0x60, v200
	v_sub_u32_e32 v206, v1, v11
	v_xad_u32 v6, v6, v2, 0
	v_xad_u32 v7, v7, v2, 0
	v_xad_u32 v8, v8, v2, 0
	v_xad_u32 v2, v200, v2, 0
	v_lshlrev_b32_e32 v9, 8, v1
	v_mov_b32_e32 v199, v3
	v_add_u32_e32 v208, v2, v9
	v_add_u32_e32 v209, v6, v9
	v_add_u32_e32 v210, v7, v9
	v_add_u32_e32 v211, v8, v9
	v_or_b32_e32 v202, v200, v9
	v_mov_b32_e32 v203, v3
	v_mov_b32_e32 v201, v3
	s_movk_i32 s40, 0x800
	s_movk_i32 s41, 0xf7ff
	s_mov_b32 s42, 0x41000000
	s_mov_b32 s18, 0x3e0293ee
	s_mov_b32 s43, 0x8000
	s_mov_b32 s44, 0xa000
	v_add_u32_e32 v212, 0, v10
	v_add_u32_e32 v213, 0, v4
	v_add_u32_e32 v214, 0, v5
	s_mov_b32 s45, 0
	v_add_u32_e32 v215, 0xfffff745, v206
	v_mov_b32_e32 v216, 0xff800000
	v_mov_b32_e32 v217, 0xf149f2ca
	s_waitcnt lgkmcnt(0)
	s_barrier
	s_branch .LBB3_5

.LBB3_14:
	s_nop 8
	v_max_f32_e32 v2, v21, v21
	v_max_f32_e32 v36, v20, v20
	v_max_f32_e32 v2, v36, v2
	v_max3_f32 v2, v2, v22, v23
	v_max3_f32 v2, v2, v24, v25
	v_max3_f32 v2, v2, v26, v27
	v_max3_f32 v2, v2, v28, v29
	v_max3_f32 v2, v2, v30, v31
	v_max3_f32 v2, v2, v32, v33
	v_max3_f32 v2, v2, v34, v35
	v_max3_f32 v2, v2, v4, v5
	v_max3_f32 v2, v2, v6, v7
	v_max3_f32 v2, v2, v8, v9
	v_max3_f32 v2, v2, v10, v11
	v_max3_f32 v2, v2, v12, v13
	v_max3_f32 v2, v2, v14, v15
	v_max3_f32 v2, v2, v16, v17
	v_max3_f32 v2, v2, v18, v19
	v_mov_b32_e32 v36, v2
	s_nop 1
	v_permlane32_swap_b32_e32 v2, v36
	v_max_f32_e32 v36, v36, v36
	v_max_f32_e32 v2, v2, v2
	v_max_f32_e32 v2, v2, v36
	v_add_f32_e32 v36, 0x7149f2ca, v2
	v_mul_f32_e32 v36, 0x3db504f3, v36
	v_cmp_ge_f32_e32 vcc, s42, v36
	s_cmp_eq_u64 vcc, exec
	s_cselect_b64 s[0:1], -1, 0
	s_andn2_b64 vcc, exec, s[34:35]
	s_cbranch_vccnz .LBB3_16
	s_waitcnt vmcnt(0)
	s_waitcnt vmcnt(3)
	ds_write_b128 v212, v[182:185] offset:16384
	s_waitcnt vmcnt(2)
	ds_write_b128 v213, v[178:181] offset:16384
	s_waitcnt vmcnt(1)
	ds_write_b128 v214, v[186:189] offset:49152
	s_waitcnt vmcnt(0)
	ds_write_b128 v214, v[190:193] offset:57344
	s_cmp_lt_u32 s59, s58
	s_cbranch_scc0 .Lwo_np_a
	v_cvt_pk_f16_f32 v246, v246, v247
	v_cvt_pk_f16_f32 v247, v248, v249
	v_cvt_pk_f16_f32 v248, v250, v251
	v_cvt_pk_f16_f32 v249, v252, v253
	s_lshl_b32 s61, s59, 13
	s_add_u32 s62, s56, s61
	s_addc_u32 s63, s57, 0
	global_store_dwordx4 v255, v[246:249], s[62:63] sc1
	s_add_i32 s59, s59, 1
.Lwo_np_a:
	s_cmp_lt_u32 s58, 16
	s_cbranch_scc0 .Lwo_ni_a
	s_lshl_b32 s61, s58, 14
	s_add_u32 s61, s61, s60
	s_add_u32 s62, s54, s61
	s_addc_u32 s63, s55, 0
	global_load_dwordx4 v[246:249], v254, s[62:63] nt
	global_load_dwordx4 v[250:253], v254, s[62:63] offset:16 nt
	s_add_i32 s58, s58, 1
.Lwo_ni_a:
.LBB3_16:
	v_max_f32_e32 v36, 0xf149f2ca, v2
	v_cndmask_b32_e64 v194, v36, v217, s[0:1]
	v_mul_f32_e32 v2, 0xbe0293ee, v194
	v_fmamk_f32 v20, v20, 0x3e0293ee, v2
	v_exp_f32_e32 v143, v20
	v_sub_f32_e32 v20, 0xf149f2ca, v36
	v_mul_f32_e32 v20, 0x3e0293ee, v20
	v_fmamk_f32 v21, v21, 0x3e0293ee, v2
	v_fmamk_f32 v22, v22, 0x3e0293ee, v2
	v_fmamk_f32 v23, v23, 0x3e0293ee, v2
	v_fmamk_f32 v24, v24, 0x3e0293ee, v2
	v_fmamk_f32 v25, v25, 0x3e0293ee, v2
	v_fmamk_f32 v26, v26, 0x3e0293ee, v2
	v_fmamk_f32 v27, v27, 0x3e0293ee, v2
	v_fmamk_f32 v28, v28, 0x3e0293ee, v2
	v_fmamk_f32 v29, v29, 0x3e0293ee, v2
	v_fmamk_f32 v30, v30, 0x3e0293ee, v2
	v_fmamk_f32 v31, v31, 0x3e0293ee, v2
	v_fmamk_f32 v32, v32, 0x3e0293ee, v2
	v_fmamk_f32 v33, v33, 0x3e0293ee, v2
	v_fmamk_f32 v34, v34, 0x3e0293ee, v2
	v_fmamk_f32 v35, v35, 0x3e0293ee, v2
	v_exp_f32_e32 v20, v20
	v_exp_f32_e32 v145, v21
	v_exp_f32_e32 v141, v22
	v_exp_f32_e32 v144, v23
	v_exp_f32_e32 v140, v24
	v_exp_f32_e32 v142, v25
	v_exp_f32_e32 v138, v26
	v_exp_f32_e32 v139, v27
	v_exp_f32_e32 v133, v28
	v_exp_f32_e32 v136, v29
	v_exp_f32_e32 v131, v30
	v_exp_f32_e32 v134, v31
	v_exp_f32_e32 v130, v32
	v_exp_f32_e32 v137, v33
	v_exp_f32_e32 v132, v34
	v_exp_f32_e32 v135, v35
	v_cndmask_b32_e64 v219, v20, 1.0, s[0:1]
	v_pk_fma_f32 v[128:129], v[18:19], s[18:19], v[2:3] op_sel_hi:[1,0,0]
	v_pk_fma_f32 v[126:127], v[16:17], s[18:19], v[2:3] op_sel_hi:[1,0,0]
	v_pk_fma_f32 v[124:125], v[14:15], s[18:19], v[2:3] op_sel_hi:[1,0,0]
	v_pk_fma_f32 v[122:123], v[12:13], s[18:19], v[2:3] op_sel_hi:[1,0,0]
	v_pk_fma_f32 v[120:121], v[10:11], s[18:19], v[2:3] op_sel_hi:[1,0,0]
	v_pk_fma_f32 v[118:119], v[8:9], s[18:19], v[2:3] op_sel_hi:[1,0,0]
	v_pk_fma_f32 v[116:117], v[6:7], s[18:19], v[2:3] op_sel_hi:[1,0,0]
	v_pk_fma_f32 v[114:115], v[4:5], s[18:19], v[2:3] op_sel_hi:[1,0,0]
	s_cmp_lt_i32 s48, 3
	s_waitcnt lgkmcnt(0)
	s_barrier
	s_cbranch_scc1 .LBB3_31
	s_add_i32 s0, s47, s51
	v_mov_b32_e32 v220, 0
	v_add_u32_e32 v221, s0, v215
	s_movk_i32 s14, 0xbf
	s_mov_b32 s51, 2
	v_mov_b32_e32 v18, 0
	v_mov_b32_e32 v19, v220
	v_mov_b32_e32 v20, v220
	v_mov_b32_e32 v21, v220
	v_mov_b32_e32 v22, v220
	v_mov_b32_e32 v23, v220
	v_mov_b32_e32 v24, v220
	v_mov_b32_e32 v25, v220
	v_mov_b32_e32 v26, v220
	v_mov_b32_e32 v27, v220
	v_mov_b32_e32 v28, v220
	v_mov_b32_e32 v29, v220
	v_mov_b32_e32 v30, v220
	v_mov_b32_e32 v31, v220
	v_mov_b32_e32 v32, v220
	v_mov_b32_e32 v33, v220
	v_mov_b32_e32 v34, 0
	v_mov_b32_e32 v35, v220
	v_mov_b32_e32 v36, v220
	v_mov_b32_e32 v37, v220
	v_mov_b32_e32 v38, v220
	v_mov_b32_e32 v39, v220
	v_mov_b32_e32 v40, v220
	v_mov_b32_e32 v41, v220
	v_mov_b32_e32 v42, v220
	v_mov_b32_e32 v43, v220
	v_mov_b32_e32 v44, v220
	v_mov_b32_e32 v45, v220
	v_mov_b32_e32 v46, v220
	v_mov_b32_e32 v47, v220
	v_mov_b32_e32 v48, v220
	v_mov_b32_e32 v49, v220
	v_mov_b32_e32 v50, 0
	v_mov_b32_e32 v51, v220
	v_mov_b32_e32 v52, v220
	v_mov_b32_e32 v53, v220
	v_mov_b32_e32 v54, v220
	v_mov_b32_e32 v55, v220
	v_mov_b32_e32 v56, v220
	v_mov_b32_e32 v57, v220
	v_mov_b32_e32 v58, v220
	v_mov_b32_e32 v59, v220
	v_mov_b32_e32 v60, v220
	v_mov_b32_e32 v61, v220
	v_mov_b32_e32 v62, v220
	v_mov_b32_e32 v63, v220
	v_mov_b32_e32 v64, v220
	v_mov_b32_e32 v65, v220
	v_mov_b32_e32 v66, 0
	v_mov_b32_e32 v67, v220
	v_mov_b32_e32 v68, v220
	v_mov_b32_e32 v69, v220
	v_mov_b32_e32 v70, v220
	v_mov_b32_e32 v71, v220
	v_mov_b32_e32 v72, v220
	v_mov_b32_e32 v73, v220
	v_mov_b32_e32 v74, v220
	v_mov_b32_e32 v75, v220
	v_mov_b32_e32 v76, v220
	v_mov_b32_e32 v77, v220
	v_mov_b32_e32 v78, v220
	v_mov_b32_e32 v79, v220
	v_mov_b32_e32 v80, v220
	v_mov_b32_e32 v81, v220
	s_branch .LBB3_19

.LBB3_21:
	ds_read_b64_tr_b16 v[118:119], v207 offset:0
	ds_read_b64_tr_b16 v[120:121], v207 offset:0x800
	ds_read_b64_tr_b16 v[122:123], v207 offset:0x1000
	ds_read_b64_tr_b16 v[124:125], v207 offset:0x1800
	ds_read_b64_tr_b16 v[126:127], v207 offset:0x2000
	ds_read_b64_tr_b16 v[128:129], v207 offset:0x2800
	ds_read_b64_tr_b16 v[130:131], v207 offset:0x3000
	ds_read_b64_tr_b16 v[132:133], v207 offset:0x3800
	s_waitcnt lgkmcnt(0)
	s_nop 0
	v_mfma_f32_32x32x16_f16 v[66:81], v[118:121], v[4:7], v[66:81]
	v_max_f32_e32 v2, v99, v99
	v_max_f32_e32 v118, v98, v98
	v_max_f32_e32 v2, v118, v2
	v_max3_f32 v2, v2, v100, v101
	v_max3_f32 v2, v2, v102, v103
	v_max3_f32 v2, v2, v104, v105
	v_max3_f32 v2, v2, v106, v107
	v_mfma_f32_32x32x16_f16 v[66:81], v[122:125], v[8:11], v[66:81]
	v_max3_f32 v2, v2, v108, v109
	v_max3_f32 v2, v2, v110, v111
	v_max3_f32 v2, v2, v112, v113
	v_mfma_f32_32x32x16_f16 v[66:81], v[126:129], v[12:15], v[66:81]
	v_mfma_f32_32x32x16_f16 v[66:81], v[130:133], v[114:117], v[66:81]
	ds_read_b64_tr_b16 v[118:119], v207 offset:0x200
	ds_read_b64_tr_b16 v[120:121], v207 offset:0xa00
	ds_read_b64_tr_b16 v[122:123], v207 offset:0x1200
	ds_read_b64_tr_b16 v[124:125], v207 offset:0x1a00
	ds_read_b64_tr_b16 v[126:127], v207 offset:0x2200
	ds_read_b64_tr_b16 v[128:129], v207 offset:0x2a00
	ds_read_b64_tr_b16 v[130:131], v207 offset:0x3200
	ds_read_b64_tr_b16 v[132:133], v207 offset:0x3a00
	s_waitcnt lgkmcnt(0)
	s_nop 0
	v_mfma_f32_32x32x16_f16 v[50:65], v[118:121], v[4:7], v[50:65]
	v_max3_f32 v2, v2, v82, v83
	v_max3_f32 v2, v2, v84, v85
	v_max3_f32 v2, v2, v86, v87
	v_max3_f32 v2, v2, v88, v89
	v_max3_f32 v2, v2, v90, v91
	v_max3_f32 v2, v2, v92, v93
	v_max3_f32 v2, v2, v94, v95
	v_mfma_f32_32x32x16_f16 v[50:65], v[122:125], v[8:11], v[50:65]
	v_max3_f32 v2, v2, v96, v97
	v_mov_b32_e32 v118, v2
	s_nop 1
	v_permlane32_swap_b32_e32 v2, v118
	v_max_f32_e32 v118, v118, v118
	v_max_f32_e32 v2, v2, v2
	v_max_f32_e32 v2, v2, v118
	v_mfma_f32_32x32x16_f16 v[50:65], v[126:129], v[12:15], v[50:65]
	v_mfma_f32_32x32x16_f16 v[50:65], v[130:133], v[114:117], v[50:65]
	ds_read_b64_tr_b16 v[118:119], v207 offset:0x400
	ds_read_b64_tr_b16 v[120:121], v207 offset:0xc00
	ds_read_b64_tr_b16 v[122:123], v207 offset:0x1400
	ds_read_b64_tr_b16 v[124:125], v207 offset:0x1c00
	ds_read_b64_tr_b16 v[126:127], v207 offset:0x2400
	ds_read_b64_tr_b16 v[128:129], v207 offset:0x2c00
	ds_read_b64_tr_b16 v[130:131], v207 offset:0x3400
	ds_read_b64_tr_b16 v[132:133], v207 offset:0x3c00
	s_waitcnt lgkmcnt(0)
	s_nop 0
	v_mfma_f32_32x32x16_f16 v[34:49], v[118:121], v[4:7], v[34:49]
	v_sub_f32_e32 v118, v2, v194
	v_mul_f32_e32 v118, 0x3db504f3, v118
	v_cmp_ge_f32_e32 vcc, s42, v118
	s_cmp_eq_u64 vcc, exec
	v_max_f32_e32 v118, v194, v194
	v_max_f32_e32 v2, v118, v2
	s_cselect_b64 vcc, -1, 0
	v_mfma_f32_32x32x16_f16 v[34:49], v[122:125], v[8:11], v[34:49]
	v_cndmask_b32_e32 v226, v2, v194, vcc
	v_sub_f32_e32 v2, v194, v226
	v_mul_f32_e32 v2, 0x3e0293ee, v2
	v_exp_f32_e32 v2, v2
	s_nop 0
	v_cndmask_b32_e64 v2, v2, 1.0, vcc
	v_mfma_f32_32x32x16_f16 v[34:49], v[126:129], v[12:15], v[34:49]
	v_mfma_f32_32x32x16_f16 v[34:49], v[130:133], v[114:117], v[34:49]
	ds_read_b64_tr_b16 v[118:119], v207 offset:0x600
	ds_read_b64_tr_b16 v[120:121], v207 offset:0xe00
	ds_read_b64_tr_b16 v[122:123], v207 offset:0x1600
	ds_read_b64_tr_b16 v[124:125], v207 offset:0x1e00
	ds_read_b64_tr_b16 v[126:127], v207 offset:0x2600
	ds_read_b64_tr_b16 v[128:129], v207 offset:0x2e00
	ds_read_b64_tr_b16 v[130:131], v207 offset:0x3600
	ds_read_b64_tr_b16 v[132:133], v207 offset:0x3e00
	s_waitcnt lgkmcnt(0)
	s_nop 0
	v_mfma_f32_32x32x16_f16 v[18:33], v[118:121], v[4:7], v[18:33]
	v_mfma_f32_32x32x16_f16 v[18:33], v[122:125], v[8:11], v[18:33]
	v_mfma_f32_32x32x16_f16 v[18:33], v[126:129], v[12:15], v[18:33]
	v_mfma_f32_32x32x16_f16 v[18:33], v[130:133], v[114:117], v[18:33]
	s_barrier
	s_waitcnt vmcnt(0)
	v_cmp_gt_f32_e32 vcc, 1.0, v2
	s_waitcnt vmcnt(3)
	ds_write_b128 v212, v[182:185]
	s_waitcnt vmcnt(2)
	ds_write_b128 v213, v[178:181]
	s_waitcnt vmcnt(1)
	ds_write_b128 v214, v[186:189] offset:32768
	s_waitcnt vmcnt(0)
	ds_write_b128 v214, v[190:193] offset:40960
	s_cmp_lt_u32 s59, s58
	s_cbranch_scc0 .Lwo_np_b
	v_cvt_pk_f16_f32 v246, v246, v247
	v_cvt_pk_f16_f32 v247, v248, v249
	v_cvt_pk_f16_f32 v248, v250, v251
	v_cvt_pk_f16_f32 v249, v252, v253
	s_lshl_b32 s61, s59, 13
	s_add_u32 s62, s56, s61
	s_addc_u32 s63, s57, 0
	global_store_dwordx4 v255, v[246:249], s[62:63] sc1
	s_add_i32 s59, s59, 1

.Lwo_ni_b:
	s_cbranch_vccz .LBB3_23
	v_pk_mul_f32 v[80:81], v[80:81], v[2:3] op_sel_hi:[1,0]
	v_pk_mul_f32 v[78:79], v[78:79], v[2:3] op_sel_hi:[1,0]
	v_pk_mul_f32 v[76:77], v[76:77], v[2:3] op_sel_hi:[1,0]
	v_pk_mul_f32 v[74:75], v[74:75], v[2:3] op_sel_hi:[1,0]
	v_pk_mul_f32 v[72:73], v[72:73], v[2:3] op_sel_hi:[1,0]
	v_pk_mul_f32 v[70:71], v[70:71], v[2:3] op_sel_hi:[1,0]
	v_pk_mul_f32 v[68:69], v[68:69], v[2:3] op_sel_hi:[1,0]
	v_pk_mul_f32 v[66:67], v[66:67], v[2:3] op_sel_hi:[1,0]
	v_pk_mul_f32 v[64:65], v[64:65], v[2:3] op_sel_hi:[1,0]
	v_pk_mul_f32 v[62:63], v[62:63], v[2:3] op_sel_hi:[1,0]
	v_pk_mul_f32 v[60:61], v[60:61], v[2:3] op_sel_hi:[1,0]
	v_pk_mul_f32 v[58:59], v[58:59], v[2:3] op_sel_hi:[1,0]
	v_pk_mul_f32 v[56:57], v[56:57], v[2:3] op_sel_hi:[1,0]
	v_pk_mul_f32 v[54:55], v[54:55], v[2:3] op_sel_hi:[1,0]
	v_pk_mul_f32 v[52:53], v[52:53], v[2:3] op_sel_hi:[1,0]
	v_pk_mul_f32 v[50:51], v[50:51], v[2:3] op_sel_hi:[1,0]
	v_pk_mul_f32 v[48:49], v[48:49], v[2:3] op_sel_hi:[1,0]
	v_pk_mul_f32 v[46:47], v[46:47], v[2:3] op_sel_hi:[1,0]
	v_pk_mul_f32 v[44:45], v[44:45], v[2:3] op_sel_hi:[1,0]
	v_pk_mul_f32 v[42:43], v[42:43], v[2:3] op_sel_hi:[1,0]
	v_pk_mul_f32 v[40:41], v[40:41], v[2:3] op_sel_hi:[1,0]
	v_pk_mul_f32 v[38:39], v[38:39], v[2:3] op_sel_hi:[1,0]
	v_pk_mul_f32 v[36:37], v[36:37], v[2:3] op_sel_hi:[1,0]
	v_pk_mul_f32 v[34:35], v[34:35], v[2:3] op_sel_hi:[1,0]
	v_pk_mul_f32 v[32:33], v[2:3], v[32:33] op_sel_hi:[0,1]
	v_pk_mul_f32 v[30:31], v[2:3], v[30:31] op_sel_hi:[0,1]
	v_pk_mul_f32 v[28:29], v[2:3], v[28:29] op_sel_hi:[0,1]
	v_pk_mul_f32 v[26:27], v[2:3], v[26:27] op_sel_hi:[0,1]
	v_pk_mul_f32 v[24:25], v[2:3], v[24:25] op_sel_hi:[0,1]
	v_pk_mul_f32 v[22:23], v[2:3], v[22:23] op_sel_hi:[0,1]
	v_pk_mul_f32 v[20:21], v[2:3], v[20:21] op_sel_hi:[0,1]
	v_pk_mul_f32 v[18:19], v[2:3], v[18:19] op_sel_hi:[0,1]

.LBB3_44:
	s_mov_b64 exec, -1
.Lwo_tail:
	s_cmp_lt_u32 s59, s58
	s_cbranch_scc0 .Lwo_np_t
	s_waitcnt vmcnt(0)
	v_cvt_pk_f16_f32 v246, v246, v247
	v_cvt_pk_f16_f32 v247, v248, v249
	v_cvt_pk_f16_f32 v248, v250, v251
	v_cvt_pk_f16_f32 v249, v252, v253
	s_lshl_b32 s61, s59, 13
	s_add_u32 s62, s56, s61
	s_addc_u32 s63, s57, 0
	global_store_dwordx4 v255, v[246:249], s[62:63] sc1
	s_add_i32 s59, s59, 1
.Lwo_np_t:
	s_cmp_lt_u32 s58, 16
	s_cbranch_scc0 .Lwo_ni_t
	s_lshl_b32 s61, s58, 14
	s_add_u32 s61, s61, s60
	s_add_u32 s62, s54, s61
	s_addc_u32 s63, s55, 0
	global_load_dwordx4 v[246:249], v254, s[62:63] nt
	global_load_dwordx4 v[250:253], v254, s[62:63] offset:16 nt
	s_add_i32 s58, s58, 1
	s_branch .Lwo_tail
.Lwo_ni_t:
	s_cmp_lt_u32 s59, s58
	s_cbranch_scc1 .Lwo_tail

	.amdhsa_kernel _Z11attn_kernelPKDF16_PDF16_
		.amdhsa_group_segment_fixed_size 0
		.amdhsa_private_segment_fixed_size 0
		.amdhsa_kernarg_size 272
		.amdhsa_user_sgpr_count 2
		.amdhsa_user_sgpr_dispatch_ptr 0
		.amdhsa_user_sgpr_queue_ptr 0
		.amdhsa_user_sgpr_kernarg_segment_ptr 1
		.amdhsa_user_sgpr_dispatch_id 0
		.amdhsa_user_sgpr_kernarg_preload_length 0
		.amdhsa_user_sgpr_kernarg_preload_offset 0
		.amdhsa_user_sgpr_private_segment_size 0
		.amdhsa_uses_dynamic_stack 0
		.amdhsa_enable_private_segment 0
		.amdhsa_system_sgpr_workgroup_id_x 1
		.amdhsa_system_sgpr_workgroup_id_y 0
		.amdhsa_system_sgpr_workgroup_id_z 0
		.amdhsa_system_sgpr_workgroup_info 0
		.amdhsa_system_vgpr_workitem_id 0
		.amdhsa_next_free_vgpr 256
		.amdhsa_next_free_sgpr 64
		.amdhsa_accum_offset 256
		.amdhsa_reserve_vcc 1
		.amdhsa_float_round_mode_32 0
		.amdhsa_float_round_mode_16_64 0
		.amdhsa_float_denorm_mode_32 3
		.amdhsa_float_denorm_mode_16_64 3
		.amdhsa_dx10_clamp 1
		.amdhsa_ieee_mode 1
		.amdhsa_fp16_overflow 0
		.amdhsa_tg_split 0
		.amdhsa_exception_fp_ieee_invalid_op 0
		.amdhsa_exception_fp_denorm_src 0
		.amdhsa_exception_fp_ieee_div_zero 0
		.amdhsa_exception_fp_ieee_overflow 0
		.amdhsa_exception_fp_ieee_underflow 0
		.amdhsa_exception_fp_ieee_inexact 0
		.amdhsa_exception_int_div_zero 0
	.end_amdhsa_kernel

amdhsa.kernels:
  - .agpr_count:     0
    .args:
      - .actual_access:  read_only
        .address_space:  global
        .offset:         0
        .size:           8
        .value_kind:     global_buffer
      - .actual_access:  read_only
        .address_space:  global
        .offset:         8
        .size:           8
        .value_kind:     global_buffer
      - .actual_access:  read_only
        .address_space:  global
        .offset:         16
        .size:           8
        .value_kind:     global_buffer
      - .actual_access:  read_only
        .address_space:  global
        .offset:         24
        .size:           8
        .value_kind:     global_buffer
      - .actual_access:  read_only
        .address_space:  global
        .offset:         32
        .size:           8
        .value_kind:     global_buffer
      - .address_space:  global
        .offset:         40
        .size:           8
        .value_kind:     global_buffer
      - .address_space:  global
        .offset:         48
        .size:           8
        .value_kind:     global_buffer
      - .address_space:  global
        .offset:         56
        .size:           8
        .value_kind:     global_buffer
      - .actual_access:  write_only
        .address_space:  global
        .offset:         64
        .size:           8
        .value_kind:     global_buffer
    .group_segment_fixed_size: 0
    .kernarg_segment_align: 8
    .kernarg_segment_size: 72
    .language:       OpenCL C
    .language_version:
      - 2
      - 0
    .max_flat_workgroup_size: 256
    .name:           _Z10cvt_kernelPKfS0_S0_S0_S0_PDF16_S1_S1_P15HIP_vector_typeIfLj2EE
    .private_segment_fixed_size: 0
    .sgpr_count:     30
    .sgpr_spill_count: 0
    .symbol:         _Z10cvt_kernelPKfS0_S0_S0_S0_PDF16_S1_S1_P15HIP_vector_typeIfLj2EE.kd
    .uniform_work_group_size: 1
    .uses_dynamic_stack: false
    .vgpr_count:     21
    .vgpr_spill_count: 0
    .wavefront_size: 64
  - .agpr_count:     0
    .args:
      - .address_space:  global
        .offset:         0
        .size:           8
        .value_kind:     global_buffer
      - .address_space:  global
        .offset:         8
        .size:           8
        .value_kind:     global_buffer
      - .address_space:  global
        .offset:         16
        .size:           8
        .value_kind:     global_buffer
      - .offset:         24
        .size:           4
        .value_kind:     by_value
      - .offset:         28
        .size:           4
        .value_kind:     by_value
      - .offset:         32
        .size:           4
        .value_kind:     by_value
    .group_segment_fixed_size: 0
    .kernarg_segment_align: 8
    .kernarg_segment_size: 36
    .language:       OpenCL C
    .language_version:
      - 2
      - 0
    .max_flat_workgroup_size: 512
    .name:           _Z15gemm_out_kernelPKDF16_S0_Pfiii
    .private_segment_fixed_size: 0
    .sgpr_count:     42
    .sgpr_spill_count: 0
    .symbol:         _Z15gemm_out_kernelPKDF16_S0_Pfiii.kd
    .uniform_work_group_size: 1
    .uses_dynamic_stack: false
    .vgpr_count:     247
    .vgpr_spill_count: 0
    .wavefront_size: 64
  - .agpr_count:     0
    .args:
      - .address_space:  global
        .offset:         0
        .size:           8
        .value_kind:     global_buffer
      - .address_space:  global
        .offset:         8
        .size:           8
        .value_kind:     global_buffer
      - .address_space:  global
        .offset:         16
        .size:           8
        .value_kind:     global_buffer
      - .actual_access:  read_only
        .address_space:  global
        .offset:         24
        .size:           8
        .value_kind:     global_buffer
      - .actual_access:  read_only
        .address_space:  global
        .offset:         32
        .size:           8
        .value_kind:     global_buffer
      - .actual_access:  read_only
        .address_space:  global
        .offset:         40
        .size:           8
        .value_kind:     global_buffer
    .group_segment_fixed_size: 0
    .kernarg_segment_align: 8
    .kernarg_segment_size: 48
    .language:       OpenCL C
    .language_version:
      - 2
      - 0
    .max_flat_workgroup_size: 512
    .name:           _Z15gemm_qkv_kernelPKDF16_S0_PDF16_PKfS3_PK15HIP_vector_typeIfLj2EE
    .private_segment_fixed_size: 0
    .sgpr_count:     49
    .sgpr_spill_count: 0
    .symbol:         _Z15gemm_qkv_kernelPKDF16_S0_PDF16_PKfS3_PK15HIP_vector_typeIfLj2EE.kd
    .uniform_work_group_size: 1
    .uses_dynamic_stack: false
    .vgpr_count:     226
    .vgpr_spill_count: 0
    .wavefront_size: 64
  - .agpr_count:     0
    .args:
      - .actual_access:  read_only
        .address_space:  global
        .offset:         0
        .size:           8
        .value_kind:     global_buffer
      - .actual_access:  write_only
        .address_space:  global
        .offset:         8
        .size:           8
        .value_kind:     global_buffer
      - .offset:         16
        .size:           4
        .value_kind:     hidden_block_count_x
      - .offset:         20
        .size:           4
        .value_kind:     hidden_block_count_y
      - .offset:         24
        .size:           4
        .value_kind:     hidden_block_count_z
      - .offset:         28
        .size:           2
        .value_kind:     hidden_group_size_x
      - .offset:         30
        .size:           2
        .value_kind:     hidden_group_size_y
      - .offset:         32
        .size:           2
        .value_kind:     hidden_group_size_z
      - .offset:         34
        .size:           2
        .value_kind:     hidden_remainder_x
      - .offset:         36
        .size:           2
        .value_kind:     hidden_remainder_y
      - .offset:         38
        .size:           2
        .value_kind:     hidden_remainder_z
      - .offset:         56
        .size:           8
        .value_kind:     hidden_global_offset_x
      - .offset:         64
        .size:           8
        .value_kind:     hidden_global_offset_y
      - .offset:         72
        .size:           8
        .value_kind:     hidden_global_offset_z
      - .offset:         80
        .size:           2
        .value_kind:     hidden_grid_dims
      - .offset:         136
        .size:           4
        .value_kind:     hidden_dynamic_lds_size
    .group_segment_fixed_size: 0
    .kernarg_segment_align: 8
    .kernarg_segment_size: 272
    .language:       OpenCL C
    .language_version:
      - 2
      - 0
    .max_flat_workgroup_size: 512
    .name:           _Z11attn_kernelPKDF16_PDF16_
    .private_segment_fixed_size: 0
    .sgpr_count:     70
    .sgpr_spill_count: 0
    .symbol:         _Z11attn_kernelPKDF16_PDF16_.kd
    .uniform_work_group_size: 1
    .uses_dynamic_stack: false
    .vgpr_count:     256
    .vgpr_spill_count: 0
    .wavefront_size: 64
